# P9 gate/up GEMM: first K iteration peeled out of the rotated loop (accumulators start from srcC=0, 128 zeroing v_mov per unit removed)
# speedup vs baseline: 1.0053x; 1.0053x over previous
; #define PG8_STAGE2(bufoff, gbase, v0, v1) do { \
;         __builtin_amdgcn_global_load_lds((const unsigned*)((const char*)(gbase) + (v0)), (LAS unsigned*)(lds + (bufoff) + ldsw), 16, 0, 0); \
;         __builtin_amdgcn_global_load_lds((const unsigned*)((const char*)(gbase) + (v1)), (LAS unsigned*)(lds + (bufoff) + ldsw + 8192), 16, 0, 0); } while (0)
; #define PG8_LDA(dst, b, h) do { _Pragma("unroll") for (int m = 0; m < 4; ++m) _Pragma("unroll") for (int k = 0; k < 2; ++k) dst[m][k] = *(const LAS bf16x8*)(lds + PG8_SA(b, h) + aoff + m * 2048 + k * 1024); } while (0)
; #define PG8_LDB(dst, b, h) do { _Pragma("unroll") for (int n = 0; n < 2; ++n) _Pragma("unroll") for (int k = 0; k < 2; ++k) dst[n][k] = *(const LAS bf16x8*)(lds + PG8_SB(b, h) + boff + n * 2048 + k * 1024); } while (0)
; #define PG8_BAR __builtin_amdgcn_s_barrier()
; template <class Epi, class Sched, bool ALIGN_EPI, bool SP2, bool GATHER>
; DI void gemm_phase(LAS unsigned char* lds, const Gemm g, const Sched& S, const Epi& E) {
;     ...
;     for (;;) {
;         const bool has_next = S.next(ui + 1, nxt);
;         const char* nA = (has_next && !GATHER) ? (const char*)g.A + (size_t)nxt.pm * tstep : cA; const char* nB = has_next ? (const char*)g.Bt + (size_t)nxt.pn * tstep : cB;
;         if constexpr (GATHER) { if (has_next) { PG8_GATHER(nxt, gN); } else {
; #pragma unroll
;             for (int h = 0; h < 2; ++h) { gN[h][0] = gC[h][0]; gN[h][1] = gC[h][1]; } } }
;         for (int t = 0; t < nt; t += 2) {
;             if constexpr (Epi::MID_T >= 0) { if (t == Epi::MID_T) { E.mid(acc, cur, wr, wc, fr, fq); PG8_SCHED; } }
;             const bool last = (t == nt - 2);
;             const char* a1 = cA + (size_t)(t + 1) * kstep;
;             const char* a2 = last ? nA : cA + (size_t)(t + 2) * kstep; const char* b2 = last ? nB : cB + (size_t)(t + 2) * kstep;
;             const char* a3 = a2 + kstep; const char* b3 = b2 + kstep;
;             unsigned x00 = gC[0][0], x01 = gC[0][1], x10 = gC[1][0], x11 = gC[1][1];
;             if constexpr (GATHER) { if (last) { x00 = gN[0][0]; x01 = gN[0][1]; x10 = gN[1][0]; x11 = gN[1][1]; } }
;             PG8_LDB(B0, 0, 0); PG8_LDB(B1, 0, 1); PG8_SCHED; PG8_LDA(At, 0, 0); PG8_STAGE2(PG8_SA(1, 1), a1 + hstepA, gC[1][0], gC[1][1]);
;             PG8_WAIT_V(8); PG8_WAIT_L(0); PG8_BAR; PG8_MMA(0, 0, At, B0); PG8_MMA(0, 1, At, B1); PG8_BAR; PG8_SCHED;
.LBB0_904:
	s_ashr_i32 s29, s28, 31
	s_lshl_b64 s[30:31], s[28:29], 20
	s_add_u32 s30, s39, s30
	s_addc_u32 s31, s44, s31
	s_and_b64 s[40:41], s[40:41], exec
	s_cselect_b32 s29, s31, s37
	s_cselect_b32 s64, s30, s36
	s_add_u32 s65, s36, 0x100
	v_mov_b32_e32 v141, v135
	v_mov_b32_e32 v144, v136
	v_mov_b32_e32 v145, v135
	v_mov_b32_e32 v139, v135
	v_mov_b32_e32 v136, v2
	v_mov_b32_e32 v137, v135
	s_addc_u32 s66, s37, 0
	s_mov_b32 s67, -2
	s_mov_b64 s[36:37], s[16:17]
	s_cmp_eq_u32 s67, 28
	s_cselect_b64 s[40:41], -1, 0
	v_mov_b64_e32 v[146:147], v[144:145]
	v_mov_b64_e32 v[148:149], v[140:141]
	v_mov_b32_e32 v134, v143
	v_mov_b32_e32 v150, v142
	v_add_u32_e32 v151, s53, v155
	ds_read_b128 v[160:163], v151
	ds_read_b128 v[164:167], v151 offset:1024
	ds_read_b128 v[168:171], v151 offset:2048
	ds_read_b128 v[172:175], v151 offset:3072
	v_add_u32_e32 v151, s54, v155
	ds_read_b128 v[176:179], v151
	ds_read_b128 v[180:183], v151 offset:1024
	ds_read_b128 v[184:187], v151 offset:2048
	ds_read_b128 v[188:191], v151 offset:3072
	s_add_u32 s42, s36, 0x80
	s_addc_u32 s43, s37, 0
	s_and_b64 s[40:41], s[40:41], exec
	s_cselect_b32 s43, s5, s43
	s_cselect_b32 s42, s4, s42
	s_cselect_b32 s41, s29, s66
	s_cselect_b32 s40, s64, s65
	v_lshl_add_u64 v[224:225], s[36:37], 0, v[140:141]
	s_add_i32 m0, s35, 0xc000
	ds_read_b128 v[192:195], v157
	ds_read_b128 v[196:199], v157 offset:1024
	ds_read_b128 v[200:203], v157 offset:2048
	ds_read_b128 v[204:207], v157 offset:3072
	ds_read_b128 v[208:211], v157 offset:4096
	ds_read_b128 v[212:215], v157 offset:5120
	ds_read_b128 v[216:219], v157 offset:6144
	ds_read_b128 v[220:223], v157 offset:7168
	global_load_lds_dwordx4 v[224:225], off
	v_lshl_add_u64 v[224:225], s[36:37], 0, v[144:145]
	s_add_i32 m0, s35, 0xe000
	s_nop 0
	global_load_lds_dwordx4 v[224:225], off
	s_waitcnt vmcnt(8)
	s_waitcnt lgkmcnt(0)
	s_barrier
	s_setprio 1
	s_waitcnt lgkmcnt(0)
	v_mfma_f32_16x16x32_bf16 v[122:125], v[160:163], v[192:195], 0
	v_mfma_f32_16x16x32_bf16 v[126:129], v[168:171], v[192:195], 0
	v_mfma_f32_16x16x32_bf16 v[106:109], v[160:163], v[200:203], 0
	v_mfma_f32_16x16x32_bf16 v[110:113], v[168:171], v[200:203], 0
	v_mfma_f32_16x16x32_bf16 v[90:93], v[160:163], v[208:211], 0
	v_mfma_f32_16x16x32_bf16 v[94:97], v[168:171], v[208:211], 0
	v_mfma_f32_16x16x32_bf16 v[74:77], v[160:163], v[216:219], 0
	v_mfma_f32_16x16x32_bf16 v[78:81], v[168:171], v[216:219], 0
	v_mfma_f32_16x16x32_bf16 v[122:125], v[164:167], v[196:199], v[122:125]
	v_mfma_f32_16x16x32_bf16 v[126:129], v[172:175], v[196:199], v[126:129]
	v_mfma_f32_16x16x32_bf16 v[106:109], v[164:167], v[204:207], v[106:109]
	v_mfma_f32_16x16x32_bf16 v[110:113], v[172:175], v[204:207], v[110:113]
	v_mfma_f32_16x16x32_bf16 v[90:93], v[164:167], v[212:215], v[90:93]
	v_mfma_f32_16x16x32_bf16 v[94:97], v[172:175], v[212:215], v[94:97]
	v_mfma_f32_16x16x32_bf16 v[74:77], v[164:167], v[220:223], v[74:77]
	v_mfma_f32_16x16x32_bf16 v[78:81], v[172:175], v[220:223], v[78:81]
	s_setprio 0
	s_setprio 1
	v_mfma_f32_16x16x32_bf16 v[114:117], v[176:179], v[192:195], 0
	v_mfma_f32_16x16x32_bf16 v[118:121], v[184:187], v[192:195], 0
	v_mfma_f32_16x16x32_bf16 v[98:101], v[176:179], v[200:203], 0
	v_mfma_f32_16x16x32_bf16 v[102:105], v[184:187], v[200:203], 0
	v_mfma_f32_16x16x32_bf16 v[82:85], v[176:179], v[208:211], 0
	v_mfma_f32_16x16x32_bf16 v[86:89], v[184:187], v[208:211], 0
	v_mfma_f32_16x16x32_bf16 v[66:69], v[176:179], v[216:219], 0
	v_mfma_f32_16x16x32_bf16 v[70:73], v[184:187], v[216:219], 0
	v_mfma_f32_16x16x32_bf16 v[114:117], v[180:183], v[196:199], v[114:117]
	v_mfma_f32_16x16x32_bf16 v[118:121], v[188:191], v[196:199], v[118:121]
	v_mfma_f32_16x16x32_bf16 v[98:101], v[180:183], v[204:207], v[98:101]
	v_mfma_f32_16x16x32_bf16 v[102:105], v[188:191], v[204:207], v[102:105]
	v_mfma_f32_16x16x32_bf16 v[82:85], v[180:183], v[212:215], v[82:85]
	v_mfma_f32_16x16x32_bf16 v[86:89], v[188:191], v[212:215], v[86:89]
	v_mfma_f32_16x16x32_bf16 v[66:69], v[180:183], v[220:223], v[66:69]
	v_mfma_f32_16x16x32_bf16 v[70:73], v[188:191], v[220:223], v[70:73]
	s_setprio 0
	s_barrier
	s_add_i32 s68, s53, s45
	v_lshl_add_u64 v[224:225], s[40:41], 0, v[132:133]
	s_mov_b32 m0, s68
	ds_read_b128 v[192:195], v157 offset:16384
	ds_read_b128 v[196:199], v157 offset:17408
	ds_read_b128 v[200:203], v157 offset:18432
	ds_read_b128 v[204:207], v157 offset:19456
	ds_read_b128 v[208:211], v157 offset:20480
	ds_read_b128 v[212:215], v157 offset:21504
	ds_read_b128 v[216:219], v157 offset:22528
	ds_read_b128 v[220:223], v157 offset:23552
	global_load_lds_dwordx4 v[224:225], off
	s_add_i32 m0, s68, 0x2000
	s_add_u32 s68, s40, 0x80000
	v_lshl_add_u64 v[226:227], s[40:41], 0, v[130:131]
	s_addc_u32 s69, s41, 0
	s_add_i32 s70, s54, s45
	global_load_lds_dwordx4 v[226:227], off
	v_lshl_add_u64 v[228:229], s[68:69], 0, v[132:133]
	s_mov_b32 m0, s70
	v_mov_b32_e32 v151, v135
	global_load_lds_dwordx4 v[228:229], off
	v_lshl_add_u64 v[228:229], s[68:69], 0, v[130:131]
	s_add_i32 m0, s70, 0x2000
	s_nop 0
	global_load_lds_dwordx4 v[228:229], off
	s_mov_b32 m0, s35
	v_lshl_add_u64 v[228:229], s[42:43], 0, v[134:135]
	global_load_lds_dwordx4 v134, s[42:43]
	s_mov_b32 m0, s46
	s_nop 0
	global_load_lds_dwordx4 v150, s[42:43]
	s_waitcnt vmcnt(8)
	s_waitcnt lgkmcnt(0)
	v_lshl_add_u64 v[150:151], s[42:43], 0, v[150:151]
	s_barrier
; #define PG8_STAGE2(bufoff, gbase, v0, v1) do { \
;         __builtin_amdgcn_global_load_lds((const unsigned*)((const char*)(gbase) + (v0)), (LAS unsigned*)(lds + (bufoff) + ldsw), 16, 0, 0); \
;         __builtin_amdgcn_global_load_lds((const unsigned*)((const char*)(gbase) + (v1)), (LAS unsigned*)(lds + (bufoff) + ldsw + 8192), 16, 0, 0); } while (0)
; #define PG8_LDA(dst, b, h) do { _Pragma("unroll") for (int m = 0; m < 4; ++m) _Pragma("unroll") for (int k = 0; k < 2; ++k) dst[m][k] = *(const LAS bf16x8*)(lds + PG8_SA(b, h) + aoff + m * 2048 + k * 1024); } while (0)
; #define PG8_LDB(dst, b, h) do { _Pragma("unroll") for (int n = 0; n < 2; ++n) _Pragma("unroll") for (int k = 0; k < 2; ++k) dst[n][k] = *(const LAS bf16x8*)(lds + PG8_SB(b, h) + boff + n * 2048 + k * 1024); } while (0)
; #define PG8_MMA(ai, bj, At, Bt) do { __builtin_amdgcn_s_setprio(1); _Pragma("unroll") for (int m = 0; m < 4; ++m) _Pragma("unroll") for (int n = 0; n < 2; ++n) _Pragma("unroll") for (int k = 0; k < 2; ++k) \
;         acc[ai][bj][m][n] = __builtin_amdgcn_mfma_f32_16x16x32_bf16(Bt[n][k], At[m][k], acc[ai][bj][m][n], 0, 0, 0); __builtin_amdgcn_s_setprio(0); } while (0)
; #define PG8_WAIT_V(n) asm volatile("s_waitcnt vmcnt(" #n ")" ::: "memory")
; #define PG8_WAIT_L(n) asm volatile("s_waitcnt lgkmcnt(" #n ")" ::: "memory")
; #define PG8_BAR __builtin_amdgcn_s_barrier()
; #define PG8_SCHED __builtin_amdgcn_sched_barrier(0)
; template <class Epi, class Sched, bool ALIGN_EPI, bool SP2, bool GATHER>
; DI void gemm_phase(LAS unsigned char* lds, const Gemm g, const Sched& S, const Epi& E) {
;     ...
;             PG8_WAIT_V(8); PG8_WAIT_L(0); PG8_BAR; PG8_MMA(1, 0, At, B0); PG8_MMA(1, 1, At, B1); PG8_BAR; PG8_SCHED;
;             PG8_LDB(B0, 1, 0); PG8_LDB(B1, 1, 1); PG8_SCHED; PG8_LDA(At, 1, 0); PG8_STAGE2(PG8_SA(0, 1), a2 + hstepA, x10, x11);
;             PG8_WAIT_V(8); PG8_WAIT_L(0); PG8_BAR; PG8_MMA(0, 0, At, B0); PG8_MMA(0, 1, At, B1); PG8_BAR; PG8_SCHED;
	s_setprio 1
	s_waitcnt lgkmcnt(0)
	v_mfma_f32_16x16x32_bf16 v[58:61], v[160:163], v[192:195], 0
	v_mfma_f32_16x16x32_bf16 v[62:65], v[168:171], v[192:195], 0
	v_mfma_f32_16x16x32_bf16 v[42:45], v[160:163], v[200:203], 0
	v_mfma_f32_16x16x32_bf16 v[46:49], v[168:171], v[200:203], 0
	v_mfma_f32_16x16x32_bf16 v[26:29], v[160:163], v[208:211], 0
	v_mfma_f32_16x16x32_bf16 v[30:33], v[168:171], v[208:211], 0
	v_mfma_f32_16x16x32_bf16 v[10:13], v[160:163], v[216:219], 0
	v_mfma_f32_16x16x32_bf16 v[14:17], v[168:171], v[216:219], 0
	v_mfma_f32_16x16x32_bf16 v[58:61], v[164:167], v[196:199], v[58:61]
	v_mfma_f32_16x16x32_bf16 v[62:65], v[172:175], v[196:199], v[62:65]
	v_mfma_f32_16x16x32_bf16 v[42:45], v[164:167], v[204:207], v[42:45]
	v_mfma_f32_16x16x32_bf16 v[46:49], v[172:175], v[204:207], v[46:49]
	v_mfma_f32_16x16x32_bf16 v[26:29], v[164:167], v[212:215], v[26:29]
	v_mfma_f32_16x16x32_bf16 v[30:33], v[172:175], v[212:215], v[30:33]
	v_mfma_f32_16x16x32_bf16 v[10:13], v[164:167], v[220:223], v[10:13]
	v_mfma_f32_16x16x32_bf16 v[14:17], v[172:175], v[220:223], v[14:17]
	s_setprio 0
	s_setprio 1
	v_mfma_f32_16x16x32_bf16 v[50:53], v[176:179], v[192:195], 0
	v_mfma_f32_16x16x32_bf16 v[54:57], v[184:187], v[192:195], 0
	v_mfma_f32_16x16x32_bf16 v[34:37], v[176:179], v[200:203], 0
	v_mfma_f32_16x16x32_bf16 v[38:41], v[184:187], v[200:203], 0
	v_mfma_f32_16x16x32_bf16 v[18:21], v[176:179], v[208:211], 0
	v_mfma_f32_16x16x32_bf16 v[22:25], v[184:187], v[208:211], 0
	v_mfma_f32_16x16x32_bf16 v[2:5], v[176:179], v[216:219], 0
	v_mfma_f32_16x16x32_bf16 v[6:9], v[184:187], v[216:219], 0
	v_mfma_f32_16x16x32_bf16 v[50:53], v[180:183], v[196:199], v[50:53]
	v_mfma_f32_16x16x32_bf16 v[54:57], v[188:191], v[196:199], v[54:57]
	v_mfma_f32_16x16x32_bf16 v[34:37], v[180:183], v[204:207], v[34:37]
	v_mfma_f32_16x16x32_bf16 v[38:41], v[188:191], v[204:207], v[38:41]
	v_mfma_f32_16x16x32_bf16 v[18:21], v[180:183], v[212:215], v[18:21]
	v_mfma_f32_16x16x32_bf16 v[22:25], v[188:191], v[212:215], v[22:25]
	v_mfma_f32_16x16x32_bf16 v[2:5], v[180:183], v[220:223], v[2:5]
	v_mfma_f32_16x16x32_bf16 v[6:9], v[188:191], v[220:223], v[6:9]
	s_setprio 0
	s_barrier
	s_add_i32 s68, 0, 0x18000
	v_add_u32_e32 v134, s68, v155
	s_add_i32 s69, 0, 0x1c000
	ds_read_b128 v[160:163], v134
	ds_read_b128 v[164:167], v134 offset:1024
	ds_read_b128 v[168:171], v134 offset:2048
	ds_read_b128 v[172:175], v134 offset:3072
	v_add_u32_e32 v134, s69, v155
	ds_read_b128 v[176:179], v134
	ds_read_b128 v[180:183], v134 offset:1024
	ds_read_b128 v[184:187], v134 offset:2048
	ds_read_b128 v[188:191], v134 offset:3072
	s_mov_b32 m0, s47
	v_lshl_add_u64 v[148:149], s[42:43], 0, v[148:149]
	ds_read_b128 v[192:195], v157 offset:32768
	ds_read_b128 v[196:199], v157 offset:33792
	ds_read_b128 v[200:203], v157 offset:34816
	ds_read_b128 v[204:207], v157 offset:35840
	ds_read_b128 v[208:211], v157 offset:36864
	ds_read_b128 v[212:215], v157 offset:37888
	ds_read_b128 v[216:219], v157 offset:38912
	ds_read_b128 v[220:223], v157 offset:39936
	global_load_lds_dwordx4 v[148:149], off
	v_lshl_add_u64 v[146:147], s[42:43], 0, v[146:147]
	s_mov_b32 m0, s48
	s_nop 0
	global_load_lds_dwordx4 v[146:147], off
	s_waitcnt vmcnt(8)
	s_waitcnt lgkmcnt(0)
	s_barrier
	s_setprio 1
	s_waitcnt lgkmcnt(0)
	v_mfma_f32_16x16x32_bf16 v[122:125], v[160:163], v[192:195], v[122:125]
	v_mfma_f32_16x16x32_bf16 v[126:129], v[168:171], v[192:195], v[126:129]
	v_mfma_f32_16x16x32_bf16 v[106:109], v[160:163], v[200:203], v[106:109]
	v_mfma_f32_16x16x32_bf16 v[110:113], v[168:171], v[200:203], v[110:113]
	v_mfma_f32_16x16x32_bf16 v[90:93], v[160:163], v[208:211], v[90:93]
	v_mfma_f32_16x16x32_bf16 v[94:97], v[168:171], v[208:211], v[94:97]
	v_mfma_f32_16x16x32_bf16 v[74:77], v[160:163], v[216:219], v[74:77]
	v_mfma_f32_16x16x32_bf16 v[78:81], v[168:171], v[216:219], v[78:81]
	v_mfma_f32_16x16x32_bf16 v[122:125], v[164:167], v[196:199], v[122:125]
	v_mfma_f32_16x16x32_bf16 v[126:129], v[172:175], v[196:199], v[126:129]
	v_mfma_f32_16x16x32_bf16 v[106:109], v[164:167], v[204:207], v[106:109]
	v_mfma_f32_16x16x32_bf16 v[110:113], v[172:175], v[204:207], v[110:113]
	v_mfma_f32_16x16x32_bf16 v[90:93], v[164:167], v[212:215], v[90:93]
	v_mfma_f32_16x16x32_bf16 v[94:97], v[172:175], v[212:215], v[94:97]
	v_mfma_f32_16x16x32_bf16 v[74:77], v[164:167], v[220:223], v[74:77]
	v_mfma_f32_16x16x32_bf16 v[78:81], v[172:175], v[220:223], v[78:81]
	s_setprio 0
	s_setprio 1
	v_mfma_f32_16x16x32_bf16 v[114:117], v[176:179], v[192:195], v[114:117]
	v_mfma_f32_16x16x32_bf16 v[118:121], v[184:187], v[192:195], v[118:121]
	v_mfma_f32_16x16x32_bf16 v[98:101], v[176:179], v[200:203], v[98:101]
	v_mfma_f32_16x16x32_bf16 v[102:105], v[184:187], v[200:203], v[102:105]
	v_mfma_f32_16x16x32_bf16 v[82:85], v[176:179], v[208:211], v[82:85]
	v_mfma_f32_16x16x32_bf16 v[86:89], v[184:187], v[208:211], v[86:89]
	v_mfma_f32_16x16x32_bf16 v[66:69], v[176:179], v[216:219], v[66:69]
	v_mfma_f32_16x16x32_bf16 v[70:73], v[184:187], v[216:219], v[70:73]
	v_mfma_f32_16x16x32_bf16 v[114:117], v[180:183], v[196:199], v[114:117]
	v_mfma_f32_16x16x32_bf16 v[118:121], v[188:191], v[196:199], v[118:121]
	v_mfma_f32_16x16x32_bf16 v[98:101], v[180:183], v[204:207], v[98:101]
	v_mfma_f32_16x16x32_bf16 v[102:105], v[188:191], v[204:207], v[102:105]
	v_mfma_f32_16x16x32_bf16 v[82:85], v[180:183], v[212:215], v[82:85]
	v_mfma_f32_16x16x32_bf16 v[86:89], v[188:191], v[212:215], v[86:89]
	v_mfma_f32_16x16x32_bf16 v[66:69], v[180:183], v[220:223], v[66:69]
	v_mfma_f32_16x16x32_bf16 v[70:73], v[188:191], v[220:223], v[70:73]
	s_setprio 0
	s_barrier
; #define PG8_STAGE2(bufoff, gbase, v0, v1) do { \
;         __builtin_amdgcn_global_load_lds((const unsigned*)((const char*)(gbase) + (v0)), (LAS unsigned*)(lds + (bufoff) + ldsw), 16, 0, 0); \
;         __builtin_amdgcn_global_load_lds((const unsigned*)((const char*)(gbase) + (v1)), (LAS unsigned*)(lds + (bufoff) + ldsw + 8192), 16, 0, 0); } while (0)
; #define PG8_STAGE(bufoff, gbase, voff) PG8_STAGE2(bufoff, gbase, (voff)[0], (voff)[1])
; #define PG8_LDA(dst, b, h) do { _Pragma("unroll") for (int m = 0; m < 4; ++m) _Pragma("unroll") for (int k = 0; k < 2; ++k) dst[m][k] = *(const LAS bf16x8*)(lds + PG8_SA(b, h) + aoff + m * 2048 + k * 1024); } while (0)
; #define PG8_MMA(ai, bj, At, Bt) do { __builtin_amdgcn_s_setprio(1); _Pragma("unroll") for (int m = 0; m < 4; ++m) _Pragma("unroll") for (int n = 0; n < 2; ++n) _Pragma("unroll") for (int k = 0; k < 2; ++k) \
;         acc[ai][bj][m][n] = __builtin_amdgcn_mfma_f32_16x16x32_bf16(Bt[n][k], At[m][k], acc[ai][bj][m][n], 0, 0, 0); __builtin_amdgcn_s_setprio(0); } while (0)
; #define PG8_WAIT_V(n) asm volatile("s_waitcnt vmcnt(" #n ")" ::: "memory")
; #define PG8_WAIT_L(n) asm volatile("s_waitcnt lgkmcnt(" #n ")" ::: "memory")
; #define PG8_BAR __builtin_amdgcn_s_barrier()
; #define PG8_SCHED __builtin_amdgcn_sched_barrier(0)
; template <class Epi, class Sched, bool ALIGN_EPI, bool SP2, bool GATHER>
; DI void gemm_phase(LAS unsigned char* lds, const Gemm g, const Sched& S, const Epi& E) {
;     ...
;             PG8_LDA(At, 1, 1); PG8_STAGE(PG8_SB(1, 0), b3, voffB); PG8_STAGE(PG8_SB(1, 1), b3 + hstep, voffB); PG8_STAGE2(PG8_SA(1, 0), a3, x00, x01);
;             PG8_WAIT_V(8); PG8_WAIT_L(0); PG8_BAR; PG8_MMA(1, 0, At, B0); PG8_MMA(1, 1, At, B1); PG8_BAR; PG8_SCHED;
;         }
	s_add_i32 s42, s68, s45
	v_lshl_add_u64 v[220:221], v[224:225], 0, s[14:15]
	s_mov_b32 m0, s42
	ds_read_b128 v[146:149], v157 offset:49152
	ds_read_b128 v[192:195], v157 offset:50176
	ds_read_b128 v[196:199], v157 offset:51200
	ds_read_b128 v[200:203], v157 offset:52224
	ds_read_b128 v[204:207], v157 offset:53248
	ds_read_b128 v[208:211], v157 offset:54272
	ds_read_b128 v[212:215], v157 offset:55296
	ds_read_b128 v[216:219], v157 offset:56320
	global_load_lds_dwordx4 v[220:221], off
	s_add_i32 m0, s42, 0x2000
	s_add_u32 s40, s40, 0x80080
	v_lshl_add_u64 v[220:221], v[226:227], 0, s[14:15]
	s_addc_u32 s41, s41, 0
	s_add_i32 s42, s69, s45
	global_load_lds_dwordx4 v[220:221], off
	v_lshl_add_u64 v[220:221], s[40:41], 0, v[132:133]
	s_mov_b32 m0, s42
	v_lshl_add_u64 v[150:151], v[150:151], 0, s[14:15]
	global_load_lds_dwordx4 v[220:221], off
	v_lshl_add_u64 v[220:221], s[40:41], 0, v[130:131]
	s_add_i32 m0, s42, 0x2000
	s_nop 0
	global_load_lds_dwordx4 v[220:221], off
	v_lshl_add_u64 v[220:221], v[228:229], 0, s[14:15]
	s_mov_b32 m0, s50
	s_nop 0
	global_load_lds_dwordx4 v[220:221], off
	s_mov_b32 m0, s51
	s_nop 0
	global_load_lds_dwordx4 v[150:151], off
	s_waitcnt vmcnt(8)
	s_waitcnt lgkmcnt(0)
	s_barrier
	s_setprio 1
	s_waitcnt lgkmcnt(0)
	v_mfma_f32_16x16x32_bf16 v[58:61], v[160:163], v[146:149], v[58:61]
	v_mfma_f32_16x16x32_bf16 v[62:65], v[168:171], v[146:149], v[62:65]
	v_mfma_f32_16x16x32_bf16 v[42:45], v[160:163], v[196:199], v[42:45]
	v_mfma_f32_16x16x32_bf16 v[46:49], v[168:171], v[196:199], v[46:49]
	v_mfma_f32_16x16x32_bf16 v[26:29], v[160:163], v[204:207], v[26:29]
	v_mfma_f32_16x16x32_bf16 v[30:33], v[168:171], v[204:207], v[30:33]
	v_mfma_f32_16x16x32_bf16 v[10:13], v[160:163], v[212:215], v[10:13]
	v_mfma_f32_16x16x32_bf16 v[14:17], v[168:171], v[212:215], v[14:17]
	v_mfma_f32_16x16x32_bf16 v[58:61], v[164:167], v[192:195], v[58:61]
	v_mfma_f32_16x16x32_bf16 v[62:65], v[172:175], v[192:195], v[62:65]
	v_mfma_f32_16x16x32_bf16 v[42:45], v[164:167], v[200:203], v[42:45]
	v_mfma_f32_16x16x32_bf16 v[46:49], v[172:175], v[200:203], v[46:49]
	v_mfma_f32_16x16x32_bf16 v[26:29], v[164:167], v[208:211], v[26:29]
	v_mfma_f32_16x16x32_bf16 v[30:33], v[172:175], v[208:211], v[30:33]
	v_mfma_f32_16x16x32_bf16 v[10:13], v[164:167], v[216:219], v[10:13]
	v_mfma_f32_16x16x32_bf16 v[14:17], v[172:175], v[216:219], v[14:17]
	s_setprio 0
	s_setprio 1
	v_mfma_f32_16x16x32_bf16 v[50:53], v[176:179], v[146:149], v[50:53]
	v_mfma_f32_16x16x32_bf16 v[54:57], v[184:187], v[146:149], v[54:57]
	v_mfma_f32_16x16x32_bf16 v[34:37], v[176:179], v[196:199], v[34:37]
	v_mfma_f32_16x16x32_bf16 v[38:41], v[184:187], v[196:199], v[38:41]
	v_mfma_f32_16x16x32_bf16 v[18:21], v[176:179], v[204:207], v[18:21]
	v_mfma_f32_16x16x32_bf16 v[22:25], v[184:187], v[204:207], v[22:25]
	v_mfma_f32_16x16x32_bf16 v[2:5], v[176:179], v[212:215], v[2:5]
	v_mfma_f32_16x16x32_bf16 v[6:9], v[184:187], v[212:215], v[6:9]
	v_mfma_f32_16x16x32_bf16 v[50:53], v[180:183], v[192:195], v[50:53]
	v_mfma_f32_16x16x32_bf16 v[54:57], v[188:191], v[192:195], v[54:57]
	v_mfma_f32_16x16x32_bf16 v[34:37], v[180:183], v[200:203], v[34:37]
	v_mfma_f32_16x16x32_bf16 v[38:41], v[188:191], v[200:203], v[38:41]
	v_mfma_f32_16x16x32_bf16 v[18:21], v[180:183], v[208:211], v[18:21]
	v_mfma_f32_16x16x32_bf16 v[22:25], v[188:191], v[208:211], v[22:25]
	v_mfma_f32_16x16x32_bf16 v[2:5], v[180:183], v[216:219], v[2:5]
	v_mfma_f32_16x16x32_bf16 v[6:9], v[188:191], v[216:219], v[6:9]
	s_setprio 0
	s_barrier
	s_add_i32 s67, s67, 2
	s_add_u32 s36, s36, 0x100
	s_addc_u32 s37, s37, 0
	s_add_u32 s65, s65, 0x100
	s_addc_u32 s66, s66, 0
	s_cmp_gt_u32 s67, 29
	s_cbranch_scc1 .LBB0_908
	s_branch .LBB0_906
